# P7: x1 row loads marked nt (streaming) so the per-batch adaLN parameter vectors stay in L1
# baseline (speedup 1.0000x reference)
.LBB0_682:
	v_lshl_add_u64 v[2:3], s[76:77], 0, v[28:29]
	v_add_co_u32_e32 v30, vcc, 0x54768000, v2
	s_add_i32 s22, s14, s15
	s_nop 0
	v_addc_co_u32_e32 v31, vcc, 0, v3, vcc
	global_load_dwordx2 v[226:227], v[30:31], off nt
	global_load_dwordx2 v[228:229], v[30:31], off offset:512 nt
	global_load_dwordx2 v[230:231], v[30:31], off offset:1024 nt
	global_load_dwordx2 v[232:233], v[30:31], off offset:1536 nt
	global_load_dwordx2 v[234:235], v[30:31], off offset:2048 nt
	global_load_dwordx2 v[236:237], v[30:31], off offset:2560 nt
	global_load_dwordx2 v[238:239], v[30:31], off offset:3072 nt
	global_load_dwordx2 v[240:241], v[30:31], off offset:3584 nt
	s_add_i32 s98, s22, 1
	s_ashr_i32 s99, s98, 31
	s_lshl_b64 s[98:99], s[98:99], 12
	v_lshl_add_u64 v[252:253], v[22:23], 0, s[98:99]
	global_load_dwordx2 v[242:243], v[252:253], off nt
	global_load_dwordx2 v[244:245], v[252:253], off offset:512 nt
	global_load_dwordx2 v[246:247], v[252:253], off offset:1024 nt
	global_load_dwordx2 v[248:249], v[252:253], off offset:1536 nt
	global_load_dwordx2 v[250:251], v[252:253], off offset:2048 nt
	s_ashr_i32 s0, s22, 13
	s_mulk_i32 s0, 0x3000
	s_ashr_i32 s1, s0, 31
	s_lshl_b64 s[0:1], s[0:1], 2
	s_add_u32 s20, s3, s0
	s_addc_u32 s21, s24, s1
	s_add_u32 s0, s20, 0x6000
	s_addc_u32 s1, s21, 0
	s_add_u32 s20, s20, 0x8000
	s_addc_u32 s21, s21, 0
	s_waitcnt vmcnt(12)
	v_and_b32_e32 v3, 0xffff0000, v226
	s_waitcnt vmcnt(11)
	v_and_b32_e32 v57, 0xffff0000, v228
	v_lshlrev_b32_e32 v2, 16, v226
	v_mul_f32_e32 v34, v3, v3
	v_lshlrev_b32_e32 v56, 16, v228
	v_mul_f32_e32 v32, v57, v57
	v_lshlrev_b32_e32 v4, 16, v227
	v_fmac_f32_e32 v34, v2, v2
	v_lshlrev_b32_e32 v58, 16, v229
	v_fmac_f32_e32 v32, v56, v56
	v_and_b32_e32 v5, 0xffff0000, v227
	v_fmac_f32_e32 v34, v4, v4
	v_and_b32_e32 v59, 0xffff0000, v229
	v_fmac_f32_e32 v32, v58, v58
	v_fmac_f32_e32 v34, v5, v5
	v_fmac_f32_e32 v32, v59, v59
	v_add_f32_e32 v34, v34, v32
	s_waitcnt vmcnt(10)
	v_and_b32_e32 v53, 0xffff0000, v230
	v_lshlrev_b32_e32 v52, 16, v230
	v_mul_f32_e32 v32, v53, v53
	v_lshlrev_b32_e32 v54, 16, v231
	v_fmac_f32_e32 v32, v52, v52
	v_and_b32_e32 v55, 0xffff0000, v231
	v_fmac_f32_e32 v32, v54, v54
	v_fmac_f32_e32 v32, v55, v55
	v_add_f32_e32 v34, v34, v32
	s_waitcnt vmcnt(9)
	v_and_b32_e32 v49, 0xffff0000, v232
	v_lshlrev_b32_e32 v48, 16, v232
	v_mul_f32_e32 v32, v49, v49
	v_lshlrev_b32_e32 v50, 16, v233
	v_fmac_f32_e32 v32, v48, v48
	v_and_b32_e32 v51, 0xffff0000, v233
	v_fmac_f32_e32 v32, v50, v50
	v_fmac_f32_e32 v32, v51, v51
	v_add_f32_e32 v36, v34, v32
	s_waitcnt vmcnt(8)
	v_and_b32_e32 v42, 0xffff0000, v234
	s_waitcnt vmcnt(7)
	v_and_b32_e32 v43, 0xffff0000, v236
	v_lshlrev_b32_e32 v41, 16, v236
	v_lshlrev_b32_e32 v40, 16, v234
	v_lshlrev_b32_e32 v44, 16, v235
	v_and_b32_e32 v46, 0xffff0000, v235
	v_pk_mul_f32 v[32:33], v[42:43], v[42:43]
	v_lshlrev_b32_e32 v45, 16, v237
	v_pk_fma_f32 v[32:33], v[40:41], v[40:41], v[32:33]
	v_and_b32_e32 v47, 0xffff0000, v237
	v_pk_fma_f32 v[32:33], v[44:45], v[44:45], v[32:33]
	s_nop 0
	v_pk_fma_f32 v[32:33], v[46:47], v[46:47], v[32:33]
	s_nop 0
	v_add_f32_e32 v32, v36, v32
	global_load_dwordx4 v[214:217], v202, s[0:1]
	global_load_dwordx4 v[218:221], v202, s[20:21]
	global_load_dwordx4 v[222:225], v[8:9], off
	v_add_f32_e32 v38, v32, v33
	s_waitcnt vmcnt(9)
	v_and_b32_e32 v32, 0xffff0000, v238
	s_waitcnt vmcnt(8)
	v_and_b32_e32 v33, 0xffff0000, v240
	v_lshlrev_b32_e32 v31, 16, v240
	v_lshlrev_b32_e32 v30, 16, v238
	v_lshlrev_b32_e32 v34, 16, v239
	v_and_b32_e32 v36, 0xffff0000, v239
	v_pk_mul_f32 v[60:61], v[32:33], v[32:33]
	v_lshlrev_b32_e32 v35, 16, v241
	v_pk_fma_f32 v[60:61], v[30:31], v[30:31], v[60:61]
	v_and_b32_e32 v37, 0xffff0000, v241
	v_pk_fma_f32 v[60:61], v[34:35], v[34:35], v[60:61]
	global_load_dwordx2 v[226:227], v[252:253], off offset:2560 nt
	global_load_dwordx2 v[228:229], v[252:253], off offset:3072 nt
	global_load_dwordx2 v[230:231], v[252:253], off offset:3584 nt
	s_waitcnt vmcnt(4)
	v_pk_add_f32 v[218:219], v[218:219], 1.0 op_sel_hi:[1,0]
	v_pk_fma_f32 v[60:61], v[36:37], v[36:37], v[60:61]
	s_nop 0
	v_add_f32_e32 v38, v38, v60
	v_add_f32_e32 v38, v38, v61
	ds_bpermute_b32 v60, v189, v38
	s_waitcnt lgkmcnt(0)
	v_add_f32_e32 v38, v38, v60
	ds_bpermute_b32 v60, v192, v38
	s_waitcnt lgkmcnt(0)
	v_add_f32_e32 v38, v38, v60
	ds_bpermute_b32 v60, v193, v38
	s_waitcnt lgkmcnt(0)
	v_add_f32_e32 v38, v38, v60
	ds_bpermute_b32 v60, v194, v38
	s_waitcnt lgkmcnt(0)
	v_add_f32_e32 v38, v38, v60
	ds_bpermute_b32 v60, v195, v38
	s_waitcnt lgkmcnt(0)
	v_add_f32_e32 v38, v38, v60
	ds_bpermute_b32 v60, v196, v38
	s_waitcnt lgkmcnt(0)
	v_add_f32_e32 v38, v38, v60
	v_fmamk_f32 v38, v38, 0x3a000000, v201
	v_cmp_gt_f32_e32 vcc, s27, v38
	v_mul_f32_e32 v60, 0x4b800000, v38
	s_nop 0
	v_cndmask_b32_e32 v38, v38, v60, vcc
	v_rsq_f32_e32 v38, v38
	s_nop 0
	v_mul_f32_e32 v60, 0x45800000, v38
	v_cndmask_b32_e32 v38, v38, v60, vcc
	v_pk_mul_f32 v[2:3], v[2:3], v[38:39] op_sel_hi:[1,0]
	v_pk_mul_f32 v[4:5], v[4:5], v[38:39] op_sel_hi:[1,0]
	s_waitcnt vmcnt(3)
	v_pk_mul_f32 v[2:3], v[222:223], v[2:3]
	v_pk_mul_f32 v[4:5], v[224:225], v[4:5]
	v_pk_fma_f32 v[2:3], v[218:219], v[2:3], v[214:215]
	v_mov_b32_e32 v214, 0
	v_cvt_pk_fp8_f32 v214, v2, v3
	v_pk_add_f32 v[60:61], v[220:221], 1.0 op_sel_hi:[1,0]
	v_pk_mul_f32 v[56:57], v[56:57], v[38:39] op_sel_hi:[1,0]
	v_pk_fma_f32 v[4:5], v[60:61], v[4:5], v[216:217]
	v_lshl_add_u64 v[60:61], s[76:77], 0, v[26:27]
	v_cvt_pk_fp8_f32 v214, v4, v5 op_sel:[0,0,1]
	v_add_co_u32_e32 v60, vcc, s28, v60
	ds_write_b128 v199, v[2:5]
	s_nop 0
	v_addc_co_u32_e32 v61, vcc, 0, v61, vcc
	s_nop 1
	v_mov_b32_e32 v240, v214
	global_load_dwordx4 v[2:5], v203, s[0:1]
	s_nop 0
	global_load_dwordx4 v[214:217], v203, s[20:21]
	global_load_dwordx4 v[218:221], v[8:9], off offset:1024
	global_store_dword v[60:61], v240, off
	v_pk_mul_f32 v[58:59], v[58:59], v[38:39] op_sel_hi:[1,0]
	v_pk_mul_f32 v[52:53], v[52:53], v[38:39] op_sel_hi:[1,0]
	v_pk_mul_f32 v[54:55], v[54:55], v[38:39] op_sel_hi:[1,0]
	v_pk_mul_f32 v[48:49], v[48:49], v[38:39] op_sel_hi:[1,0]
	v_pk_mul_f32 v[50:51], v[50:51], v[38:39] op_sel_hi:[1,0]
	s_waitcnt vmcnt(2)
	v_pk_add_f32 v[214:215], v[214:215], 1.0 op_sel_hi:[1,0]
	s_waitcnt vmcnt(1)
	v_pk_mul_f32 v[56:57], v[218:219], v[56:57]
	v_pk_mul_f32 v[58:59], v[220:221], v[58:59]
	v_pk_fma_f32 v[2:3], v[214:215], v[56:57], v[2:3]
	v_mov_b32_e32 v56, 0
	v_cvt_pk_fp8_f32 v56, v2, v3
	v_pk_add_f32 v[216:217], v[216:217], 1.0 op_sel_hi:[1,0]
	s_nop 0
	v_pk_fma_f32 v[4:5], v[216:217], v[58:59], v[4:5]
	ds_write_b128 v199, v[2:5] offset:1024
	v_cvt_pk_fp8_f32 v56, v4, v5 op_sel:[0,0,1]
	s_nop 1
	v_mov_b32_e32 v240, v56
	global_load_dwordx4 v[2:5], v204, s[0:1]
	s_nop 0
	global_load_dwordx4 v[56:59], v204, s[20:21]
	global_load_dwordx4 v[214:217], v[8:9], off offset:2048
	global_store_dword v[60:61], v240, off offset:256
	s_waitcnt vmcnt(2)
	v_pk_add_f32 v[56:57], v[56:57], 1.0 op_sel_hi:[1,0]
	s_waitcnt vmcnt(1)
	v_pk_mul_f32 v[52:53], v[214:215], v[52:53]
	v_pk_mul_f32 v[54:55], v[216:217], v[54:55]
	v_pk_fma_f32 v[2:3], v[56:57], v[52:53], v[2:3]
	v_mov_b32_e32 v52, 0
	v_cvt_pk_fp8_f32 v52, v2, v3
	v_pk_add_f32 v[58:59], v[58:59], 1.0 op_sel_hi:[1,0]
	s_nop 0
	v_pk_fma_f32 v[4:5], v[58:59], v[54:55], v[4:5]
	ds_write_b128 v199, v[2:5] offset:2048
	v_cvt_pk_fp8_f32 v52, v4, v5 op_sel:[0,0,1]
	s_nop 1
	v_mov_b32_e32 v240, v52
	global_load_dwordx4 v[2:5], v205, s[0:1]
	s_nop 0
	global_load_dwordx4 v[52:55], v205, s[20:21]
	global_load_dwordx4 v[56:59], v[8:9], off offset:3072
	global_store_dword v[60:61], v240, off offset:512
	s_waitcnt vmcnt(2)
	v_pk_add_f32 v[52:53], v[52:53], 1.0 op_sel_hi:[1,0]
	s_waitcnt vmcnt(1)
	v_pk_mul_f32 v[48:49], v[48:49], v[56:57]
	v_pk_mul_f32 v[50:51], v[50:51], v[58:59]
	v_pk_fma_f32 v[2:3], v[52:53], v[48:49], v[2:3]
	v_mov_b32_e32 v48, 0
	v_cvt_pk_fp8_f32 v48, v2, v3
	v_pk_add_f32 v[54:55], v[54:55], 1.0 op_sel_hi:[1,0]
	v_mov_b32_e32 v58, v40
	v_pk_fma_f32 v[4:5], v[54:55], v[50:51], v[4:5]
	ds_write_b128 v199, v[2:5] offset:3072
	v_cvt_pk_fp8_f32 v48, v4, v5 op_sel:[0,0,1]
	v_mov_b32_e32 v59, v42
	v_pk_mul_f32 v[58:59], v[58:59], v[38:39] op_sel_hi:[1,0]
	v_mov_b32_e32 v40, 0
	s_nop 1
	v_mov_b32_e32 v240, v48
	global_load_dwordx4 v[2:5], v206, s[0:1]
	s_nop 0
	global_load_dwordx4 v[48:51], v206, s[20:21]
	global_load_dwordx4 v[52:55], v[10:11], off
	global_store_dword v[60:61], v240, off offset:768
	v_mov_b32_e32 v56, v44
	v_mov_b32_e32 v57, v46
	v_pk_mul_f32 v[56:57], v[56:57], v[38:39] op_sel_hi:[1,0]
	v_mov_b32_e32 v42, v41
	v_mov_b32_e32 v46, v45
	v_pk_mul_f32 v[44:45], v[46:47], v[38:39] op_sel_hi:[1,0]
	s_waitcnt vmcnt(2)
	v_pk_add_f32 v[48:49], v[48:49], 1.0 op_sel_hi:[1,0]
	s_waitcnt vmcnt(1)
	v_pk_mul_f32 v[52:53], v[58:59], v[52:53]
	v_pk_mul_f32 v[54:55], v[56:57], v[54:55]
	v_pk_fma_f32 v[2:3], v[48:49], v[52:53], v[2:3]
	v_pk_add_f32 v[50:51], v[50:51], 1.0 op_sel_hi:[1,0]
	v_cvt_pk_fp8_f32 v40, v2, v3
	v_pk_fma_f32 v[4:5], v[50:51], v[54:55], v[4:5]
	ds_write_b128 v199, v[2:5] offset:4096
	v_cvt_pk_fp8_f32 v40, v4, v5 op_sel:[0,0,1]
	s_nop 1
	v_mov_b32_e32 v240, v40
	global_load_dwordx4 v[2:5], v207, s[0:1]
	global_load_dwordx4 v[48:51], v207, s[20:21]
	global_load_dwordx4 v[52:55], v[12:13], off
	global_store_dword v[60:61], v240, off offset:1024
	v_pk_mul_f32 v[40:41], v[42:43], v[38:39] op_sel_hi:[1,0]
	s_waitcnt vmcnt(2)
	v_pk_add_f32 v[46:47], v[48:49], 1.0 op_sel_hi:[1,0]
	s_waitcnt vmcnt(1)
	v_pk_mul_f32 v[40:41], v[40:41], v[52:53]
	v_pk_mul_f32 v[42:43], v[44:45], v[54:55]
	v_pk_fma_f32 v[2:3], v[46:47], v[40:41], v[2:3]
	v_mov_b32_e32 v40, 0
	v_cvt_pk_fp8_f32 v40, v2, v3
	v_pk_add_f32 v[44:45], v[50:51], 1.0 op_sel_hi:[1,0]
	v_mov_b32_e32 v50, v30
	v_pk_fma_f32 v[4:5], v[44:45], v[42:43], v[4:5]
	ds_write_b128 v199, v[2:5] offset:5120
	v_cvt_pk_fp8_f32 v40, v4, v5 op_sel:[0,0,1]
	v_mov_b32_e32 v51, v32
	v_pk_mul_f32 v[50:51], v[50:51], v[38:39] op_sel_hi:[1,0]
	v_mov_b32_e32 v30, 0
	s_nop 1
	v_mov_b32_e32 v240, v40
	global_load_dwordx4 v[2:5], v208, s[0:1]
	s_nop 0
	global_load_dwordx4 v[40:43], v208, s[20:21]
	global_load_dwordx4 v[44:47], v[14:15], off
	global_store_dword v[60:61], v240, off offset:1280
	v_mov_b32_e32 v48, v34
	v_mov_b32_e32 v49, v36
	v_pk_mul_f32 v[48:49], v[48:49], v[38:39] op_sel_hi:[1,0]
	v_mov_b32_e32 v32, v31
	v_mov_b32_e32 v36, v35
	v_pk_mul_f32 v[34:35], v[36:37], v[38:39] op_sel_hi:[1,0]
	s_waitcnt vmcnt(2)
	v_pk_add_f32 v[40:41], v[40:41], 1.0 op_sel_hi:[1,0]
	s_waitcnt vmcnt(1)
	v_pk_mul_f32 v[44:45], v[50:51], v[44:45]
	v_pk_mul_f32 v[46:47], v[48:49], v[46:47]
	v_pk_fma_f32 v[2:3], v[40:41], v[44:45], v[2:3]
	v_pk_add_f32 v[42:43], v[42:43], 1.0 op_sel_hi:[1,0]
	v_cvt_pk_fp8_f32 v30, v2, v3
	v_pk_fma_f32 v[4:5], v[42:43], v[46:47], v[4:5]
	ds_write_b128 v199, v[2:5] offset:6144
	v_cvt_pk_fp8_f32 v30, v4, v5 op_sel:[0,0,1]
	s_nop 1
	v_mov_b32_e32 v240, v30
	global_load_dwordx4 v[2:5], v209, s[0:1]
	global_load_dwordx4 v[40:43], v209, s[20:21]
	global_load_dwordx4 v[44:47], v[16:17], off
	global_store_dword v[60:61], v240, off offset:1536
	v_pk_mul_f32 v[30:31], v[32:33], v[38:39] op_sel_hi:[1,0]
	s_add_i32 s0, s22, 1
	s_ashr_i32 s1, s0, 31
	s_lshl_b64 s[20:21], s[0:1], 12
	s_lshl_b64 s[22:23], s[0:1], 11
	s_ashr_i32 s0, s0, 13
	s_mulk_i32 s0, 0x3000
	s_ashr_i32 s1, s0, 31
	s_lshl_b64 s[0:1], s[0:1], 2
	s_waitcnt vmcnt(2)
	v_pk_add_f32 v[36:37], v[40:41], 1.0 op_sel_hi:[1,0]
	s_waitcnt vmcnt(1)
	v_pk_mul_f32 v[30:31], v[30:31], v[44:45]
	v_pk_mul_f32 v[32:33], v[34:35], v[46:47]
	v_pk_fma_f32 v[2:3], v[36:37], v[30:31], v[2:3]
	v_mov_b32_e32 v30, 0
	v_cvt_pk_fp8_f32 v30, v2, v3
	v_pk_add_f32 v[34:35], v[42:43], 1.0 op_sel_hi:[1,0]
	s_nop 0
	v_pk_fma_f32 v[4:5], v[34:35], v[32:33], v[4:5]
	ds_write_b128 v199, v[2:5] offset:7168
	v_cvt_pk_fp8_f32 v30, v4, v5 op_sel:[0,0,1]
	global_store_dword v[60:61], v30, off offset:1792
	v_lshl_add_u64 v[30:31], v[22:23], 0, s[20:21]
	s_add_u32 s20, s3, s0
	s_addc_u32 s21, s24, s1
	s_add_u32 s0, s20, 0x6000
	s_addc_u32 s1, s21, 0
	s_add_u32 s20, s20, 0x8000
	s_addc_u32 s21, s21, 0
	v_and_b32_e32 v3, 0xffff0000, v242
	v_and_b32_e32 v57, 0xffff0000, v244
	v_lshlrev_b32_e32 v2, 16, v242
	v_mul_f32_e32 v34, v3, v3
	v_lshlrev_b32_e32 v56, 16, v244
	v_mul_f32_e32 v32, v57, v57
	v_lshlrev_b32_e32 v4, 16, v243
	v_fmac_f32_e32 v34, v2, v2
	v_lshlrev_b32_e32 v58, 16, v245
	v_fmac_f32_e32 v32, v56, v56
	v_and_b32_e32 v5, 0xffff0000, v243
	v_fmac_f32_e32 v34, v4, v4
	v_and_b32_e32 v59, 0xffff0000, v245
	v_fmac_f32_e32 v32, v58, v58
	v_fmac_f32_e32 v34, v5, v5
	v_fmac_f32_e32 v32, v59, v59
	v_add_f32_e32 v34, v34, v32
	v_and_b32_e32 v53, 0xffff0000, v246
	v_lshlrev_b32_e32 v52, 16, v246
	v_mul_f32_e32 v32, v53, v53
	v_lshlrev_b32_e32 v54, 16, v247
	v_fmac_f32_e32 v32, v52, v52
	v_and_b32_e32 v55, 0xffff0000, v247
	v_fmac_f32_e32 v32, v54, v54
	v_fmac_f32_e32 v32, v55, v55
	v_add_f32_e32 v34, v34, v32
	v_and_b32_e32 v49, 0xffff0000, v248
	v_lshlrev_b32_e32 v48, 16, v248
	v_mul_f32_e32 v32, v49, v49
	v_lshlrev_b32_e32 v50, 16, v249
	v_fmac_f32_e32 v32, v48, v48
	v_and_b32_e32 v51, 0xffff0000, v249
	v_fmac_f32_e32 v32, v50, v50
	v_fmac_f32_e32 v32, v51, v51
	v_add_f32_e32 v36, v34, v32
	v_and_b32_e32 v42, 0xffff0000, v250
	v_and_b32_e32 v43, 0xffff0000, v226
	v_lshlrev_b32_e32 v41, 16, v226
	v_lshlrev_b32_e32 v40, 16, v250
	v_lshlrev_b32_e32 v44, 16, v251
	v_and_b32_e32 v46, 0xffff0000, v251
	v_pk_mul_f32 v[32:33], v[42:43], v[42:43]
	v_lshlrev_b32_e32 v45, 16, v227
	v_pk_fma_f32 v[32:33], v[40:41], v[40:41], v[32:33]
	v_and_b32_e32 v47, 0xffff0000, v227
	v_pk_fma_f32 v[32:33], v[44:45], v[44:45], v[32:33]
	s_nop 0
	v_pk_fma_f32 v[32:33], v[46:47], v[46:47], v[32:33]
	s_nop 0
	v_add_f32_e32 v32, v36, v32
	global_load_dwordx4 v[214:217], v202, s[0:1]
	global_load_dwordx4 v[218:221], v202, s[20:21]
	global_load_dwordx4 v[222:225], v[8:9], off
	v_add_f32_e32 v38, v32, v33
	s_waitcnt vmcnt(4)
	v_and_b32_e32 v32, 0xffff0000, v228
	s_waitcnt vmcnt(3)
	v_and_b32_e32 v33, 0xffff0000, v230
	v_lshlrev_b32_e32 v31, 16, v230
	v_lshlrev_b32_e32 v30, 16, v228
	v_lshlrev_b32_e32 v34, 16, v229
	v_and_b32_e32 v36, 0xffff0000, v229
	v_pk_mul_f32 v[60:61], v[32:33], v[32:33]
	v_lshlrev_b32_e32 v35, 16, v231
	v_pk_fma_f32 v[60:61], v[30:31], v[30:31], v[60:61]
	v_and_b32_e32 v37, 0xffff0000, v231
	v_pk_fma_f32 v[60:61], v[34:35], v[34:35], v[60:61]
	s_waitcnt vmcnt(1)
	v_pk_add_f32 v[218:219], v[218:219], 1.0 op_sel_hi:[1,0]
	v_pk_fma_f32 v[60:61], v[36:37], v[36:37], v[60:61]
	s_nop 0
	v_add_f32_e32 v38, v38, v60
	v_add_f32_e32 v38, v38, v61
	ds_bpermute_b32 v60, v189, v38
	s_waitcnt lgkmcnt(0)
	v_add_f32_e32 v38, v38, v60
	ds_bpermute_b32 v60, v192, v38
	s_waitcnt lgkmcnt(0)
	v_add_f32_e32 v38, v38, v60
	ds_bpermute_b32 v60, v193, v38
	s_waitcnt lgkmcnt(0)
	v_add_f32_e32 v38, v38, v60
	ds_bpermute_b32 v60, v194, v38
	s_waitcnt lgkmcnt(0)
	v_add_f32_e32 v38, v38, v60
	ds_bpermute_b32 v60, v195, v38
	s_waitcnt lgkmcnt(0)
	v_add_f32_e32 v38, v38, v60
	ds_bpermute_b32 v60, v196, v38
	s_waitcnt lgkmcnt(0)
	v_add_f32_e32 v38, v38, v60
	v_fmamk_f32 v38, v38, 0x3a000000, v201
	v_cmp_gt_f32_e32 vcc, s27, v38
	v_mul_f32_e32 v60, 0x4b800000, v38
	s_nop 0
	v_cndmask_b32_e32 v38, v38, v60, vcc
	v_rsq_f32_e32 v38, v38
	s_nop 0
	v_mul_f32_e32 v60, 0x45800000, v38
	v_cndmask_b32_e32 v38, v38, v60, vcc
	v_pk_mul_f32 v[2:3], v[2:3], v[38:39] op_sel_hi:[1,0]
	v_pk_mul_f32 v[4:5], v[4:5], v[38:39] op_sel_hi:[1,0]
	s_waitcnt vmcnt(0)
	v_pk_mul_f32 v[2:3], v[222:223], v[2:3]
	v_pk_mul_f32 v[4:5], v[224:225], v[4:5]
	v_pk_fma_f32 v[2:3], v[218:219], v[2:3], v[214:215]
	v_mov_b32_e32 v214, 0
	v_cvt_pk_fp8_f32 v214, v2, v3
	v_pk_add_f32 v[60:61], v[220:221], 1.0 op_sel_hi:[1,0]
	v_pk_mul_f32 v[56:57], v[56:57], v[38:39] op_sel_hi:[1,0]
	v_pk_fma_f32 v[4:5], v[60:61], v[4:5], v[216:217]
	v_lshl_add_u64 v[60:61], v[24:25], 0, s[22:23]
	v_cvt_pk_fp8_f32 v214, v4, v5 op_sel:[0,0,1]
	ds_write_b128 v200, v[2:5]
	v_pk_mul_f32 v[58:59], v[58:59], v[38:39] op_sel_hi:[1,0]
	v_pk_mul_f32 v[52:53], v[52:53], v[38:39] op_sel_hi:[1,0]
	s_nop 1
	v_mov_b32_e32 v240, v214
	global_load_dwordx4 v[2:5], v203, s[0:1]
	s_nop 0
	global_load_dwordx4 v[214:217], v203, s[20:21]
	global_load_dwordx4 v[218:221], v[8:9], off offset:1024
	global_store_dword v[60:61], v240, off
	v_pk_mul_f32 v[54:55], v[54:55], v[38:39] op_sel_hi:[1,0]
	v_pk_mul_f32 v[48:49], v[48:49], v[38:39] op_sel_hi:[1,0]
	v_pk_mul_f32 v[50:51], v[50:51], v[38:39] op_sel_hi:[1,0]
	s_waitcnt vmcnt(2)
	v_pk_add_f32 v[214:215], v[214:215], 1.0 op_sel_hi:[1,0]
	s_waitcnt vmcnt(1)
	v_pk_mul_f32 v[56:57], v[218:219], v[56:57]
	v_pk_mul_f32 v[58:59], v[220:221], v[58:59]
	v_pk_fma_f32 v[2:3], v[214:215], v[56:57], v[2:3]
	v_mov_b32_e32 v56, 0
	v_cvt_pk_fp8_f32 v56, v2, v3
	v_pk_add_f32 v[216:217], v[216:217], 1.0 op_sel_hi:[1,0]
	s_nop 0
	v_pk_fma_f32 v[4:5], v[216:217], v[58:59], v[4:5]
	ds_write_b128 v200, v[2:5] offset:1024
	v_cvt_pk_fp8_f32 v56, v4, v5 op_sel:[0,0,1]
	s_nop 1
	v_mov_b32_e32 v240, v56
	global_load_dwordx4 v[2:5], v204, s[0:1]
	s_nop 0
	global_load_dwordx4 v[56:59], v204, s[20:21]
	global_load_dwordx4 v[214:217], v[8:9], off offset:2048
	global_store_dword v[60:61], v240, off offset:256
	s_waitcnt vmcnt(2)
	v_pk_add_f32 v[56:57], v[56:57], 1.0 op_sel_hi:[1,0]
	s_waitcnt vmcnt(1)
	v_pk_mul_f32 v[52:53], v[214:215], v[52:53]
	v_pk_mul_f32 v[54:55], v[216:217], v[54:55]
	v_pk_fma_f32 v[2:3], v[56:57], v[52:53], v[2:3]
	v_mov_b32_e32 v52, 0
	v_cvt_pk_fp8_f32 v52, v2, v3
	v_pk_add_f32 v[58:59], v[58:59], 1.0 op_sel_hi:[1,0]
	s_nop 0
	v_pk_fma_f32 v[4:5], v[58:59], v[54:55], v[4:5]
	ds_write_b128 v200, v[2:5] offset:2048
	v_cvt_pk_fp8_f32 v52, v4, v5 op_sel:[0,0,1]
	s_nop 1
	v_mov_b32_e32 v240, v52
	global_load_dwordx4 v[2:5], v205, s[0:1]
	s_nop 0
	global_load_dwordx4 v[52:55], v205, s[20:21]
	global_load_dwordx4 v[56:59], v[8:9], off offset:3072
	global_store_dword v[60:61], v240, off offset:512
	s_waitcnt vmcnt(2)
	v_pk_add_f32 v[52:53], v[52:53], 1.0 op_sel_hi:[1,0]
	s_waitcnt vmcnt(1)
	v_pk_mul_f32 v[48:49], v[48:49], v[56:57]
	v_pk_mul_f32 v[50:51], v[50:51], v[58:59]
	v_pk_fma_f32 v[2:3], v[52:53], v[48:49], v[2:3]
	v_mov_b32_e32 v48, 0
	v_cvt_pk_fp8_f32 v48, v2, v3
	v_pk_add_f32 v[54:55], v[54:55], 1.0 op_sel_hi:[1,0]
	v_mov_b32_e32 v58, v40
	v_pk_fma_f32 v[4:5], v[54:55], v[50:51], v[4:5]
	ds_write_b128 v200, v[2:5] offset:3072
	v_cvt_pk_fp8_f32 v48, v4, v5 op_sel:[0,0,1]
	v_mov_b32_e32 v59, v42
	v_pk_mul_f32 v[58:59], v[58:59], v[38:39] op_sel_hi:[1,0]
	v_mov_b32_e32 v40, 0
	s_nop 1
	v_mov_b32_e32 v240, v48
	global_load_dwordx4 v[2:5], v206, s[0:1]
	s_nop 0
	global_load_dwordx4 v[48:51], v206, s[20:21]
	global_load_dwordx4 v[52:55], v[10:11], off
	global_store_dword v[60:61], v240, off offset:768
	v_mov_b32_e32 v56, v44
	v_mov_b32_e32 v57, v46
	v_pk_mul_f32 v[56:57], v[56:57], v[38:39] op_sel_hi:[1,0]
	v_mov_b32_e32 v42, v41
	v_mov_b32_e32 v46, v45
	v_pk_mul_f32 v[44:45], v[46:47], v[38:39] op_sel_hi:[1,0]
	s_waitcnt vmcnt(2)
	v_pk_add_f32 v[48:49], v[48:49], 1.0 op_sel_hi:[1,0]
	s_waitcnt vmcnt(1)
	v_pk_mul_f32 v[52:53], v[58:59], v[52:53]
	v_pk_mul_f32 v[54:55], v[56:57], v[54:55]
	v_pk_fma_f32 v[2:3], v[48:49], v[52:53], v[2:3]
	v_pk_add_f32 v[50:51], v[50:51], 1.0 op_sel_hi:[1,0]
	v_cvt_pk_fp8_f32 v40, v2, v3
	v_pk_fma_f32 v[4:5], v[50:51], v[54:55], v[4:5]
	ds_write_b128 v200, v[2:5] offset:4096
	v_cvt_pk_fp8_f32 v40, v4, v5 op_sel:[0,0,1]
	s_nop 1
	v_mov_b32_e32 v240, v40
	global_load_dwordx4 v[2:5], v207, s[0:1]
	global_load_dwordx4 v[48:51], v207, s[20:21]
	global_load_dwordx4 v[52:55], v[12:13], off
	global_store_dword v[60:61], v240, off offset:1024
	v_pk_mul_f32 v[40:41], v[42:43], v[38:39] op_sel_hi:[1,0]
	s_waitcnt vmcnt(2)
	v_pk_add_f32 v[46:47], v[48:49], 1.0 op_sel_hi:[1,0]
	s_waitcnt vmcnt(1)
	v_pk_mul_f32 v[40:41], v[40:41], v[52:53]
	v_pk_mul_f32 v[42:43], v[44:45], v[54:55]
	v_pk_fma_f32 v[2:3], v[46:47], v[40:41], v[2:3]
	v_mov_b32_e32 v40, 0
	v_cvt_pk_fp8_f32 v40, v2, v3
	v_pk_add_f32 v[44:45], v[50:51], 1.0 op_sel_hi:[1,0]
	v_mov_b32_e32 v50, v30
	v_pk_fma_f32 v[4:5], v[44:45], v[42:43], v[4:5]
	ds_write_b128 v200, v[2:5] offset:5120
	v_cvt_pk_fp8_f32 v40, v4, v5 op_sel:[0,0,1]
	v_mov_b32_e32 v51, v32
	v_pk_mul_f32 v[50:51], v[50:51], v[38:39] op_sel_hi:[1,0]
	v_mov_b32_e32 v30, 0
	s_nop 1
	v_mov_b32_e32 v240, v40
	global_load_dwordx4 v[2:5], v208, s[0:1]
	s_nop 0
	global_load_dwordx4 v[40:43], v208, s[20:21]
	global_load_dwordx4 v[44:47], v[14:15], off
	global_store_dword v[60:61], v240, off offset:1280
	v_mov_b32_e32 v48, v34
	v_mov_b32_e32 v49, v36
	v_pk_mul_f32 v[48:49], v[48:49], v[38:39] op_sel_hi:[1,0]
	v_mov_b32_e32 v32, v31
	v_mov_b32_e32 v36, v35
	v_pk_mul_f32 v[34:35], v[36:37], v[38:39] op_sel_hi:[1,0]
	s_waitcnt vmcnt(2)
	v_pk_add_f32 v[40:41], v[40:41], 1.0 op_sel_hi:[1,0]
	s_waitcnt vmcnt(1)
	v_pk_mul_f32 v[44:45], v[50:51], v[44:45]
	v_pk_mul_f32 v[46:47], v[48:49], v[46:47]
	v_pk_fma_f32 v[2:3], v[40:41], v[44:45], v[2:3]
	v_pk_add_f32 v[42:43], v[42:43], 1.0 op_sel_hi:[1,0]
	v_cvt_pk_fp8_f32 v30, v2, v3
	v_pk_fma_f32 v[4:5], v[42:43], v[46:47], v[4:5]
	ds_write_b128 v200, v[2:5] offset:6144
	v_cvt_pk_fp8_f32 v30, v4, v5 op_sel:[0,0,1]
	s_nop 1
	v_mov_b32_e32 v240, v30
	global_load_dwordx4 v[2:5], v209, s[0:1]
	global_load_dwordx4 v[40:43], v209, s[20:21]
	global_load_dwordx4 v[44:47], v[16:17], off
	global_store_dword v[60:61], v240, off offset:1536
	v_pk_mul_f32 v[30:31], v[32:33], v[38:39] op_sel_hi:[1,0]
	s_waitcnt vmcnt(2)
	v_pk_add_f32 v[36:37], v[40:41], 1.0 op_sel_hi:[1,0]
	s_waitcnt vmcnt(1)
	v_pk_mul_f32 v[30:31], v[30:31], v[44:45]
	v_pk_mul_f32 v[32:33], v[34:35], v[46:47]
	v_pk_fma_f32 v[2:3], v[36:37], v[30:31], v[2:3]
	v_mov_b32_e32 v30, 0
	v_cvt_pk_fp8_f32 v30, v2, v3
	v_pk_add_f32 v[34:35], v[42:43], 1.0 op_sel_hi:[1,0]
	s_nop 0
	v_pk_fma_f32 v[4:5], v[34:35], v[32:33], v[4:5]
	ds_write_b128 v200, v[2:5] offset:7168
	v_cvt_pk_fp8_f32 v30, v4, v5 op_sel:[0,0,1]
	global_store_dword v[60:61], v30, off offset:1792
	s_waitcnt lgkmcnt(0)
	s_barrier
	ds_read_b128 v[2:5], v210
	s_waitcnt lgkmcnt(0)
	v_mfma_f32_16x16x4_f32 v[30:33], v2, v1, 0
	v_mfma_f32_16x16x4_f32 v[34:37], v2, v39, 0
	v_mfma_f32_16x16x4_f32 v[30:33], v3, v62, v[30:33]
	v_mfma_f32_16x16x4_f32 v[34:37], v3, v63, v[34:37]
	v_mfma_f32_16x16x4_f32 v[30:33], v4, v64, v[30:33]
	v_mfma_f32_16x16x4_f32 v[34:37], v4, v65, v[34:37]
	v_mfma_f32_16x16x4_f32 v[30:33], v5, v66, v[30:33]
	v_mfma_f32_16x16x4_f32 v[2:5], v5, v67, v[34:37]
	s_nop 7
	ds_read_b128 v[34:37], v210 offset:64
	s_waitcnt lgkmcnt(0)
	v_mfma_f32_16x16x4_f32 v[30:33], v34, v68, v[30:33]
	v_mfma_f32_16x16x4_f32 v[2:5], v34, v69, v[2:5]
	v_mfma_f32_16x16x4_f32 v[30:33], v35, v70, v[30:33]
	v_mfma_f32_16x16x4_f32 v[2:5], v35, v71, v[2:5]
	v_mfma_f32_16x16x4_f32 v[30:33], v36, v72, v[30:33]
	v_mfma_f32_16x16x4_f32 v[2:5], v36, v73, v[2:5]
	v_mfma_f32_16x16x4_f32 v[30:33], v37, v74, v[30:33]
	v_mfma_f32_16x16x4_f32 v[2:5], v37, v75, v[2:5]
	ds_read_b128 v[34:37], v210 offset:128
	s_waitcnt lgkmcnt(0)
	v_mfma_f32_16x16x4_f32 v[30:33], v34, v76, v[30:33]
	v_mfma_f32_16x16x4_f32 v[2:5], v34, v77, v[2:5]
	v_mfma_f32_16x16x4_f32 v[30:33], v35, v78, v[30:33]
	v_mfma_f32_16x16x4_f32 v[2:5], v35, v79, v[2:5]
	v_mfma_f32_16x16x4_f32 v[30:33], v36, v80, v[30:33]
	v_mfma_f32_16x16x4_f32 v[2:5], v36, v81, v[2:5]
	v_mfma_f32_16x16x4_f32 v[30:33], v37, v82, v[30:33]
	v_mfma_f32_16x16x4_f32 v[2:5], v37, v83, v[2:5]
	ds_read_b128 v[34:37], v210 offset:192
	s_waitcnt lgkmcnt(0)
	v_mfma_f32_16x16x4_f32 v[30:33], v34, v84, v[30:33]
	v_mfma_f32_16x16x4_f32 v[2:5], v34, v85, v[2:5]
	v_mfma_f32_16x16x4_f32 v[30:33], v35, v86, v[30:33]
	v_mfma_f32_16x16x4_f32 v[2:5], v35, v87, v[2:5]
	v_mfma_f32_16x16x4_f32 v[30:33], v36, v88, v[30:33]
	v_mfma_f32_16x16x4_f32 v[2:5], v36, v89, v[2:5]
	v_mfma_f32_16x16x4_f32 v[30:33], v37, v90, v[30:33]
	v_mfma_f32_16x16x4_f32 v[2:5], v37, v91, v[2:5]
	ds_read_b128 v[34:37], v210 offset:256
	s_waitcnt lgkmcnt(0)
	v_mfma_f32_16x16x4_f32 v[30:33], v34, v92, v[30:33]
	v_mfma_f32_16x16x4_f32 v[2:5], v34, v93, v[2:5]
	v_mfma_f32_16x16x4_f32 v[30:33], v35, v94, v[30:33]
	v_mfma_f32_16x16x4_f32 v[2:5], v35, v95, v[2:5]
	v_mfma_f32_16x16x4_f32 v[30:33], v36, v96, v[30:33]
	v_mfma_f32_16x16x4_f32 v[2:5], v36, v97, v[2:5]
	v_mfma_f32_16x16x4_f32 v[30:33], v37, v98, v[30:33]
	v_mfma_f32_16x16x4_f32 v[2:5], v37, v99, v[2:5]
	ds_read_b128 v[34:37], v210 offset:320
	s_waitcnt lgkmcnt(0)
	v_mfma_f32_16x16x4_f32 v[30:33], v34, v100, v[30:33]
	v_mfma_f32_16x16x4_f32 v[2:5], v34, v101, v[2:5]
	v_mfma_f32_16x16x4_f32 v[30:33], v35, v102, v[30:33]
	v_mfma_f32_16x16x4_f32 v[2:5], v35, v103, v[2:5]
	v_mfma_f32_16x16x4_f32 v[30:33], v36, v104, v[30:33]
	v_mfma_f32_16x16x4_f32 v[2:5], v36, v105, v[2:5]
	v_mfma_f32_16x16x4_f32 v[30:33], v37, v106, v[30:33]
	v_mfma_f32_16x16x4_f32 v[2:5], v37, v107, v[2:5]
	ds_read_b128 v[34:37], v210 offset:384
	s_waitcnt lgkmcnt(0)
	v_mfma_f32_16x16x4_f32 v[30:33], v34, v108, v[30:33]
	v_mfma_f32_16x16x4_f32 v[2:5], v34, v109, v[2:5]
	v_mfma_f32_16x16x4_f32 v[30:33], v35, v110, v[30:33]
	v_mfma_f32_16x16x4_f32 v[2:5], v35, v111, v[2:5]
	v_mfma_f32_16x16x4_f32 v[30:33], v36, v112, v[30:33]
	v_mfma_f32_16x16x4_f32 v[2:5], v36, v113, v[2:5]
	v_mfma_f32_16x16x4_f32 v[30:33], v37, v114, v[30:33]
	v_mfma_f32_16x16x4_f32 v[2:5], v37, v115, v[2:5]
	ds_read_b128 v[34:37], v210 offset:448
	s_waitcnt lgkmcnt(0)
	v_mfma_f32_16x16x4_f32 v[30:33], v34, v116, v[30:33]
	v_mfma_f32_16x16x4_f32 v[2:5], v34, v117, v[2:5]
	v_mfma_f32_16x16x4_f32 v[30:33], v35, v118, v[30:33]
	v_mfma_f32_16x16x4_f32 v[2:5], v35, v119, v[2:5]
	v_mfma_f32_16x16x4_f32 v[30:33], v36, v120, v[30:33]
	v_mfma_f32_16x16x4_f32 v[2:5], v36, v121, v[2:5]
	v_mfma_f32_16x16x4_f32 v[30:33], v37, v122, v[30:33]
	v_mfma_f32_16x16x4_f32 v[2:5], v37, v123, v[2:5]
	ds_read_b128 v[34:37], v210 offset:512
	s_waitcnt lgkmcnt(0)
	v_mfma_f32_16x16x4_f32 v[30:33], v34, v124, v[30:33]
	v_mfma_f32_16x16x4_f32 v[2:5], v34, v125, v[2:5]
	v_mfma_f32_16x16x4_f32 v[30:33], v35, v126, v[30:33]
	v_mfma_f32_16x16x4_f32 v[2:5], v35, v127, v[2:5]
	v_mfma_f32_16x16x4_f32 v[30:33], v36, v128, v[30:33]
	v_mfma_f32_16x16x4_f32 v[2:5], v36, v129, v[2:5]
	v_mfma_f32_16x16x4_f32 v[30:33], v37, v130, v[30:33]
	v_mfma_f32_16x16x4_f32 v[2:5], v37, v131, v[2:5]
	ds_read_b128 v[34:37], v210 offset:576
	s_waitcnt lgkmcnt(0)
	v_mfma_f32_16x16x4_f32 v[30:33], v34, v132, v[30:33]
	v_mfma_f32_16x16x4_f32 v[2:5], v34, v133, v[2:5]
	v_mfma_f32_16x16x4_f32 v[30:33], v35, v134, v[30:33]
	v_mfma_f32_16x16x4_f32 v[2:5], v35, v135, v[2:5]
	v_mfma_f32_16x16x4_f32 v[30:33], v36, v136, v[30:33]
	v_mfma_f32_16x16x4_f32 v[2:5], v36, v137, v[2:5]
	v_mfma_f32_16x16x4_f32 v[30:33], v37, v138, v[30:33]
	v_mfma_f32_16x16x4_f32 v[2:5], v37, v139, v[2:5]
	ds_read_b128 v[34:37], v210 offset:640
	s_waitcnt lgkmcnt(0)
	v_mfma_f32_16x16x4_f32 v[30:33], v34, v140, v[30:33]
	v_mfma_f32_16x16x4_f32 v[2:5], v34, v141, v[2:5]
	v_mfma_f32_16x16x4_f32 v[30:33], v35, v142, v[30:33]
	v_mfma_f32_16x16x4_f32 v[2:5], v35, v143, v[2:5]
	v_mfma_f32_16x16x4_f32 v[30:33], v36, v144, v[30:33]
	v_mfma_f32_16x16x4_f32 v[2:5], v36, v145, v[2:5]
	v_mfma_f32_16x16x4_f32 v[30:33], v37, v146, v[30:33]
	v_mfma_f32_16x16x4_f32 v[2:5], v37, v147, v[2:5]
	ds_read_b128 v[34:37], v210 offset:704
	s_waitcnt lgkmcnt(0)
	v_mfma_f32_16x16x4_f32 v[30:33], v34, v148, v[30:33]
	v_mfma_f32_16x16x4_f32 v[2:5], v34, v149, v[2:5]
	v_mfma_f32_16x16x4_f32 v[30:33], v35, v150, v[30:33]
	v_mfma_f32_16x16x4_f32 v[2:5], v35, v151, v[2:5]
	v_mfma_f32_16x16x4_f32 v[30:33], v36, v152, v[30:33]
	v_mfma_f32_16x16x4_f32 v[2:5], v36, v153, v[2:5]
	v_mfma_f32_16x16x4_f32 v[30:33], v37, v154, v[30:33]
	v_mfma_f32_16x16x4_f32 v[2:5], v37, v155, v[2:5]
	ds_read_b128 v[34:37], v210 offset:768
	s_waitcnt lgkmcnt(0)
	v_mfma_f32_16x16x4_f32 v[30:33], v34, v156, v[30:33]
	v_mfma_f32_16x16x4_f32 v[2:5], v34, v157, v[2:5]
	v_mfma_f32_16x16x4_f32 v[30:33], v35, v158, v[30:33]
	v_mfma_f32_16x16x4_f32 v[2:5], v35, v159, v[2:5]
	v_mfma_f32_16x16x4_f32 v[30:33], v36, v160, v[30:33]
	v_mfma_f32_16x16x4_f32 v[2:5], v36, v161, v[2:5]
	v_mfma_f32_16x16x4_f32 v[30:33], v37, v162, v[30:33]
	v_mfma_f32_16x16x4_f32 v[2:5], v37, v163, v[2:5]
	ds_read_b128 v[34:37], v210 offset:832
	s_waitcnt lgkmcnt(0)
	v_mfma_f32_16x16x4_f32 v[30:33], v34, v164, v[30:33]
	v_mfma_f32_16x16x4_f32 v[2:5], v34, v165, v[2:5]
	v_mfma_f32_16x16x4_f32 v[30:33], v35, v166, v[30:33]
	v_mfma_f32_16x16x4_f32 v[2:5], v35, v167, v[2:5]
	v_mfma_f32_16x16x4_f32 v[30:33], v36, v168, v[30:33]
	v_mfma_f32_16x16x4_f32 v[2:5], v36, v169, v[2:5]
	v_mfma_f32_16x16x4_f32 v[30:33], v37, v170, v[30:33]
	v_mfma_f32_16x16x4_f32 v[2:5], v37, v171, v[2:5]
	ds_read_b128 v[34:37], v210 offset:896
	s_waitcnt lgkmcnt(0)
	v_mfma_f32_16x16x4_f32 v[30:33], v34, v172, v[30:33]
	v_mfma_f32_16x16x4_f32 v[2:5], v34, v173, v[2:5]
	v_mfma_f32_16x16x4_f32 v[30:33], v35, v174, v[30:33]
	v_mfma_f32_16x16x4_f32 v[2:5], v35, v175, v[2:5]
	v_mfma_f32_16x16x4_f32 v[30:33], v36, v176, v[30:33]
	v_mfma_f32_16x16x4_f32 v[2:5], v36, v177, v[2:5]
	v_mfma_f32_16x16x4_f32 v[30:33], v37, v178, v[30:33]
	v_mfma_f32_16x16x4_f32 v[2:5], v37, v179, v[2:5]
	ds_read_b128 v[34:37], v210 offset:960
	s_waitcnt lgkmcnt(0)
	v_mfma_f32_16x16x4_f32 v[30:33], v34, v180, v[30:33]
	v_mfma_f32_16x16x4_f32 v[2:5], v34, v181, v[2:5]
	v_mfma_f32_16x16x4_f32 v[30:33], v35, v182, v[30:33]
	v_mfma_f32_16x16x4_f32 v[2:5], v35, v183, v[2:5]
	v_mfma_f32_16x16x4_f32 v[30:33], v36, v184, v[30:33]
	v_mfma_f32_16x16x4_f32 v[2:5], v36, v185, v[2:5]
	v_mfma_f32_16x16x4_f32 v[30:33], v37, v186, v[30:33]
	v_mfma_f32_16x16x4_f32 v[2:5], v37, v187, v[2:5]
	s_nop 9
	ds_write2_b32 v211, v30, v2 offset1:16
	ds_write2_b32 v211, v31, v3 offset0:32 offset1:48
	ds_write2_b32 v211, v32, v4 offset0:64 offset1:80
	ds_write2_b32 v211, v33, v5 offset0:96 offset1:112
	s_waitcnt lgkmcnt(0)
	s_barrier
	global_load_dword v4, v[18:19], off
	ds_read2st64_b32 v[2:3], v198 offset1:8
	ds_bpermute_b32 v31, v192, v197
	s_waitcnt vmcnt(0) lgkmcnt(1)
	v_add_f32_e32 v2, v4, v2
	v_add_f32_e32 v4, v2, v3
	ds_read2st64_b32 v[2:3], v198 offset0:16 offset1:24
	s_waitcnt lgkmcnt(0)
	v_add_f32_e32 v2, v4, v2
	v_add_f32_e32 v4, v2, v3
	ds_read2st64_b32 v[2:3], v198 offset0:32 offset1:40
	s_waitcnt lgkmcnt(0)
	v_add_f32_e32 v2, v4, v2
	v_add_f32_e32 v4, v2, v3
	ds_read2st64_b32 v[2:3], v198 offset0:48 offset1:56
	s_waitcnt lgkmcnt(0)
	v_add_f32_e32 v2, v4, v2
	v_add_f32_e32 v3, v2, v3
	ds_bpermute_b32 v5, v192, v3
	s_waitcnt lgkmcnt(0)
	v_cmp_lt_f32_e64 s[20:21], v3, v5
	v_cmp_nlt_f32_e32 vcc, v3, v5
	s_and_saveexec_b64 s[22:23], vcc
	v_cmp_eq_f32_e32 vcc, v3, v5
	v_cmp_lt_i32_e64 s[0:1], v31, v197
	s_and_b64 s[0:1], vcc, s[0:1]
	s_andn2_b64 s[20:21], s[20:21], exec
	s_and_b64 s[0:1], s[0:1], exec
	s_or_b64 s[20:21], s[20:21], s[0:1]
	s_or_b64 exec, exec, s[22:23]
	v_mov_b32_e32 v4, v3
	v_mov_b32_e32 v30, v3
	v_mov_b32_e32 v2, v197
	s_and_saveexec_b64 s[0:1], s[20:21]
	v_mov_b32_e32 v4, v5
	v_mov_b32_e32 v30, v5
	v_mov_b32_e32 v2, v31
	s_or_b64 exec, exec, s[0:1]
	ds_bpermute_b32 v5, v193, v4
	ds_bpermute_b32 v31, v193, v2
	s_waitcnt lgkmcnt(1)
	v_cmp_lt_f32_e64 s[20:21], v30, v5
	v_cmp_nlt_f32_e32 vcc, v30, v5
	s_and_saveexec_b64 s[22:23], vcc
	s_cbranch_execz .LBB0_688
	v_cmp_eq_f32_e32 vcc, v30, v5
	s_waitcnt lgkmcnt(0)
	v_cmp_lt_i32_e64 s[0:1], v31, v2
	s_and_b64 s[0:1], vcc, s[0:1]
	s_andn2_b64 s[20:21], s[20:21], exec
	s_and_b64 s[0:1], s[0:1], exec
	s_or_b64 s[20:21], s[20:21], s[0:1]
